# P6 K fragments of the next key block prefetched after the QK MFMAs of the current block
# baseline (speedup 1.0000x reference)
.LBB0_1661:
	s_or_b64 exec, exec, s[42:43]
	v_readfirstlane_b32 s42, v2
	s_mul_i32 s62, s42, s48
	s_add_i32 s62, s62, s2
	s_cmpk_gt_i32 s62, 0x1fff
	s_mov_b64 s[42:43], -1
	s_cbranch_scc1 .LBB0_1656
	s_ashr_i32 s42, s62, 5
	s_sub_i32 s43, 0xff, s42
	s_lshl_b32 s63, s62, 10
	s_lshl_b32 s58, s43, 5
	s_and_b32 s63, s63, 0x6000
	s_add_i32 s58, s58, s63
	v_or_b32_e32 v148, s58, v1
	s_lshl_b32 s58, s62, 7
	s_lshl_b32 s62, s62, 8
	s_and_b32 s62, s62, 0x1f00
	s_add_i32 s64, s62, s43
	s_mov_b32 s65, s59
	s_lshl_b64 s[64:65], s[64:65], 13
	v_mov_b64_e32 v[6:7], s[44:45]
	s_and_b32 s58, s58, 0x380
	s_waitcnt vmcnt(1)
	v_lshl_add_u64 v[30:31], v[140:141], 0, s[64:65]
	v_mad_u64_u32 v[6:7], s[72:73], v148, s53, v[6:7]
	global_load_dwordx4 v[2:5], v[30:31], off
	s_lshl_b32 s72, s58, 1
	s_mov_b32 s73, s59
	v_lshl_add_u64 v[6:7], v[6:7], 0, s[72:73]
	v_mov_b32_e32 v147, v139
	v_lshl_add_u64 v[6:7], v[6:7], 0, v[146:147]
	v_add_co_u32_e32 v8, vcc, s67, v6
	v_lshl_add_u64 v[36:37], v[6:7], 0, s[60:61]
	s_nop 0
	v_addc_co_u32_e32 v9, vcc, 0, v7, vcc
	global_load_dwordx4 v[82:85], v[8:9], off offset:3072
	global_load_dwordx4 v[18:21], v[30:31], off offset:1024
	global_load_dwordx4 v[86:89], v[36:37], off offset:32
	global_load_dwordx4 v[22:25], v[30:31], off offset:2048
	global_load_dwordx4 v[90:93], v[36:37], off offset:64
	global_load_dwordx4 v[26:29], v[30:31], off offset:3072
	global_load_dwordx4 v[94:97], v[36:37], off offset:96
	v_add_co_u32_e32 v30, vcc, s49, v30
	s_waitcnt vmcnt(6)
	v_mfma_f32_32x32x16_bf16 v[2:17], v[2:5], v[82:85], 0
	v_addc_co_u32_e32 v31, vcc, 0, v31, vcc
	s_waitcnt vmcnt(4)
	v_mfma_f32_32x32x16_bf16 v[2:17], v[18:21], v[86:89], v[2:17]
	global_load_dwordx4 v[18:21], v[30:31], off
	s_waitcnt vmcnt(3)
	v_mfma_f32_32x32x16_bf16 v[2:17], v[22:25], v[90:93], v[2:17]
	global_load_dwordx4 v[98:101], v[36:37], off offset:128
	global_load_dwordx4 v[22:25], v[30:31], off offset:1024
	s_waitcnt vmcnt(3)
	v_mfma_f32_32x32x16_bf16 v[2:17], v[26:29], v[94:97], v[2:17]
	s_waitcnt vmcnt(1)
	v_mfma_f32_32x32x16_bf16 v[2:17], v[18:21], v[98:101], v[2:17]
	global_load_dwordx4 v[102:105], v[36:37], off offset:160
	global_load_dwordx4 v[18:21], v[30:31], off offset:2048
	global_load_dwordx4 v[106:109], v[36:37], off offset:192
	global_load_dwordx4 v[32:35], v[30:31], off offset:3072
	global_load_dwordx4 v[110:113], v[36:37], off offset:224
	v_lshl_add_u64 v[30:31], v[142:143], 0, s[64:65]
	s_waitcnt vmcnt(4)
	v_mfma_f32_32x32x16_bf16 v[2:17], v[22:25], v[102:105], v[2:17]
	s_waitcnt vmcnt(2)
	v_mfma_f32_32x32x16_bf16 v[2:17], v[18:21], v[106:109], v[2:17]
	global_load_dwordx4 v[26:29], v[30:31], off
	global_load_dwordx4 v[22:25], v[30:31], off offset:1024
	global_load_dwordx4 v[18:21], v[30:31], off offset:2048
	s_waitcnt vmcnt(3)
	v_mfma_f32_32x32x16_bf16 v[2:17], v[32:35], v[110:113], v[2:17]
	s_nop 11
	v_mul_f32_e32 v32, 0x3e0293ee, v2
	v_exp_f32_e64 v46, -|v32|
	v_mul_f32_e32 v34, 0x3e0293ee, v4
	v_mul_f32_e32 v33, 0x3e0293ee, v3
	v_mul_f32_e32 v36, 0x3e0293ee, v6
	v_mul_f32_e32 v38, 0x3e0293ee, v8
	v_exp_f32_e64 v48, -|v34|
	v_mul_f32_e32 v37, 0x3e0293ee, v7
	v_exp_f32_e64 v47, -|v33|
	v_exp_f32_e64 v50, -|v36|
	v_exp_f32_e64 v52, -|v38|
	v_add_f32_e32 v46, 1.0, v46
	v_mul_f32_e32 v39, 0x3e0293ee, v9
	v_mul_f32_e32 v45, 0x3e0293ee, v15
	v_exp_f32_e64 v51, -|v37|
	v_log_f32_e32 v46, v46
	v_exp_f32_e64 v53, -|v39|
	v_exp_f32_e64 v59, -|v45|
	v_add_f32_e32 v48, 1.0, v48
	v_max_f32_e32 v32, 0, v32
	v_add_f32_e32 v47, 1.0, v47
	v_add_f32_e32 v50, 1.0, v50
	v_add_f32_e32 v52, 1.0, v52
	v_log_f32_e32 v48, v48
	v_mul_f32_e32 v44, 0x3e0293ee, v14
	v_add_f32_e32 v51, 1.0, v51
	v_log_f32_e32 v47, v47
	v_log_f32_e32 v50, v50
	v_log_f32_e32 v52, v52
	v_add_f32_e32 v32, v32, v46
	v_exp_f32_e64 v58, -|v44|
	v_add_f32_e32 v53, 1.0, v53
	v_log_f32_e32 v51, v51
	v_cndmask_b32_e64 v46, 0, -v32, s[8:9]
	v_fma_f32 v32, v2, s68, -v32
	v_add_f32_e32 v2, 1.0, v59
	v_max_f32_e32 v34, 0, v34
	v_log_f32_e32 v53, v53
	v_log_f32_e32 v2, v2
	v_max_f32_e32 v33, 0, v33
	v_max_f32_e32 v36, 0, v36
	v_max_f32_e32 v38, 0, v38
	v_add_f32_e32 v34, v34, v48
	v_max_f32_e32 v37, 0, v37
	v_add_f32_e32 v33, v33, v47
	v_add_f32_e32 v36, v36, v50
	v_add_f32_e32 v38, v38, v52
	v_cndmask_b32_e64 v48, 0, -v34, s[12:13]
	v_fma_f32 v34, v4, s68, -v34
	v_mul_f32_e32 v4, 0x3e0293ee, v16
	v_mul_f32_e32 v35, 0x3e0293ee, v5
	v_max_f32_e32 v39, 0, v39
	v_add_f32_e32 v58, 1.0, v58
	v_add_f32_e32 v37, v37, v51
	v_cndmask_b32_e64 v47, 0, -v33, s[10:11]
	v_fma_f32 v33, v3, s68, -v33
	v_cndmask_b32_e64 v3, 0, -v36, s[16:17]
	v_fma_f32 v36, v6, s68, -v36
	v_cndmask_b32_e64 v51, 0, -v38, s[20:21]
	v_fma_f32 v38, v8, s68, -v38
	v_exp_f32_e64 v6, -|v4|
	v_max_f32_e32 v8, 0, v45
	v_exp_f32_e64 v49, -|v35|
	v_log_f32_e32 v58, v58
	v_add_f32_e32 v39, v39, v53
	v_add_f32_e32 v2, v8, v2
	v_mul_f32_e32 v8, 0x3e0293ee, v17
	v_mul_f32_e32 v40, 0x3e0293ee, v10
	v_mul_f32_e32 v41, 0x3e0293ee, v11
	v_mul_f32_e32 v42, 0x3e0293ee, v12
	v_mul_f32_e32 v43, 0x3e0293ee, v13
	v_cndmask_b32_e64 v52, 0, -v39, s[22:23]
	v_fma_f32 v39, v9, s68, -v39
	v_exp_f32_e64 v9, -|v8|
	v_exp_f32_e64 v54, -|v40|
	v_exp_f32_e64 v55, -|v41|
	v_exp_f32_e64 v56, -|v42|
	v_exp_f32_e64 v57, -|v43|
	v_max_f32_e32 v44, 0, v44
	v_add_f32_e32 v6, 1.0, v6
	v_add_f32_e32 v49, 1.0, v49
	v_add_f32_e32 v44, v44, v58
	v_log_f32_e32 v6, v6
	v_log_f32_e32 v49, v49
	v_cndmask_b32_e64 v50, 0, -v37, s[18:19]
	v_fma_f32 v37, v7, s68, -v37
	v_cndmask_b32_e64 v7, 0, -v44, s[34:35]
	v_fma_f32 v14, v14, s68, -v44
	v_cndmask_b32_e64 v44, 0, -v2, s[36:37]
	v_fma_f32 v15, v15, s68, -v2
	v_max_f32_e32 v2, 0, v4
	v_add_f32_e32 v4, 1.0, v9
	v_add_f32_e32 v54, 1.0, v54
	v_add_f32_e32 v55, 1.0, v55
	v_add_f32_e32 v56, 1.0, v56
	v_add_f32_e32 v57, 1.0, v57
	v_log_f32_e32 v4, v4
	v_log_f32_e32 v54, v54
	v_log_f32_e32 v55, v55
	v_log_f32_e32 v56, v56
	v_log_f32_e32 v57, v57
	v_max_f32_e32 v35, 0, v35
	v_add_f32_e32 v2, v2, v6
	v_add_f32_e32 v35, v35, v49
	v_cndmask_b32_e64 v45, 0, -v2, s[38:39]
	v_fma_f32 v16, v16, s68, -v2
	v_max_f32_e32 v2, 0, v8
	v_max_f32_e32 v40, 0, v40
	v_max_f32_e32 v41, 0, v41
	v_max_f32_e32 v42, 0, v42
	v_max_f32_e32 v43, 0, v43
	v_cndmask_b32_e64 v49, 0, -v35, s[14:15]
	v_add_f32_e32 v2, v2, v4
	v_add_f32_e32 v40, v40, v54
	v_add_f32_e32 v41, v41, v55
	v_add_f32_e32 v42, v42, v56
	v_add_f32_e32 v43, v43, v57
	v_cndmask_b32_e64 v56, 0, -v2, s[40:41]
	v_fma_f32 v17, v17, s68, -v2
	v_add_f32_e32 v2, v46, v47
	v_add_f32_e32 v4, v48, v49
	v_fma_f32 v35, v5, s68, -v35
	v_cndmask_b32_e64 v5, 0, -v40, s[24:25]
	v_cndmask_b32_e64 v53, 0, -v41, s[26:27]
	v_cndmask_b32_e64 v54, 0, -v42, s[28:29]
	v_cndmask_b32_e64 v55, 0, -v43, s[30:31]
	v_add_f32_e32 v2, v2, v4
	v_add_f32_e32 v3, v3, v50
	v_add_f32_e32 v4, v51, v52
	v_add_f32_e32 v4, v3, v4
	v_add_f32_e32 v3, v5, v53
	v_add_f32_e32 v5, v54, v55
	v_add_f32_e32 v6, v3, v5
	v_add_f32_e32 v3, v7, v44
	v_add_f32_e32 v5, v45, v56
	v_add_f32_e32 v7, v3, v5
	v_fma_f32 v42, v12, s68, -v42
	v_fma_f32 v43, v13, s68, -v43
	v_mov_b32_e32 v12, v6
	v_mov_b32_e32 v13, v7
	s_nop 0
	v_permlane32_swap_b32_e32 v6, v12
	v_permlane32_swap_b32_e32 v7, v13
	v_fma_f32 v40, v10, s68, -v40
	v_mov_b32_e32 v10, v4
	v_pk_add_f32 v[6:7], v[6:7], v[12:13]
	v_fma_f32 v41, v11, s68, -v41
	v_permlane32_swap_b32_e32 v4, v10
	v_mov_b32_e32 v5, v6
	v_mov_b32_e32 v11, v7
	v_mov_b32_e32 v8, v2
	v_pk_add_f32 v[4:5], v[4:5], v[10:11]
	s_nop 0
	v_permlane32_swap_b32_e32 v2, v8
	v_mov_b32_e32 v3, v4
	v_mov_b32_e32 v9, v5
	v_pk_add_f32 v[66:67], v[2:3], v[8:9]
	v_cndmask_b32_e64 v3, 0, v8, s[6:7]
	v_add_f32_e32 v2, 0, v67
	v_add_f32_e32 v2, v3, v2
	v_add_f32_e32 v3, v49, v2
	v_add_f32_e32 v2, v35, v2
	v_add_f32_e32 v2, v153, v2
	v_add_f32_e32 v4, v48, v3
	v_exp_f32_e32 v8, v2
	v_add_f32_e32 v2, v34, v3
	v_add_f32_e32 v6, v47, v4
	v_add_f32_e32 v2, v152, v2
	v_exp_f32_e32 v3, v2
	v_add_f32_e32 v2, v33, v4
	v_add_f32_e32 v4, v32, v6
	v_add_f32_e32 v5, 0, v5
	v_cndmask_b32_e64 v6, 0, v10, s[6:7]
	v_add_f32_e32 v5, v6, v5
	v_add_f32_e32 v6, v52, v5
	v_add_f32_e32 v9, v51, v6
	v_add_f32_e32 v5, v39, v5
	v_add_f32_e32 v6, v38, v6
	v_add_f32_e32 v13, 0, v13
	v_add_f32_e32 v5, v157, v5
	v_add_f32_e32 v6, v156, v6
	v_add_f32_e32 v7, 0, v7
	v_cndmask_b32_e64 v11, 0, v12, s[6:7]
	v_cndmask_b32_e64 v13, 0, v13, s[6:7]
	v_exp_f32_e32 v5, v5
	v_exp_f32_e32 v6, v6
	v_add_f32_e32 v7, v11, v7
	v_add_f32_e32 v33, v56, v13
	v_add_f32_e32 v11, v55, v7
	v_add_f32_e32 v34, v45, v33
	v_add_f32_e32 v12, v54, v11
	v_add_f32_e32 v35, v44, v34
	v_add_f32_e32 v10, v50, v9
	v_add_f32_e32 v32, v53, v12
	v_add_f32_e32 v15, v15, v34
	v_add_f32_e32 v14, v14, v35
	v_add_f32_e32 v9, v37, v9
	v_add_f32_e32 v10, v36, v10
	v_add_f32_e32 v7, v43, v7
	v_add_f32_e32 v11, v42, v11
	v_add_f32_e32 v12, v41, v12
	v_add_f32_e32 v32, v40, v32
	v_add_f32_e32 v13, v17, v13
	v_add_f32_e32 v16, v16, v33
	v_add_f32_e32 v15, v163, v15
	v_cvt_pk_bf16_f32 v5, v6, v5
	v_add_f32_e32 v6, v162, v14
	v_add_f32_e32 v2, v151, v2
	v_add_f32_e32 v4, v150, v4
	v_add_f32_e32 v9, v155, v9
	v_add_f32_e32 v10, v154, v10
	v_add_f32_e32 v7, v161, v7
	v_add_f32_e32 v11, v160, v11
	v_add_f32_e32 v12, v159, v12
	v_add_f32_e32 v32, v158, v32
	v_add_f32_e32 v13, v165, v13
	v_add_f32_e32 v16, v164, v16
	v_exp_f32_e32 v15, v15
	v_exp_f32_e32 v6, v6
	v_exp_f32_e32 v2, v2
	v_exp_f32_e32 v4, v4
	v_exp_f32_e32 v9, v9
	v_exp_f32_e32 v10, v10
	v_exp_f32_e32 v7, v7
	v_exp_f32_e32 v11, v11
	v_exp_f32_e32 v12, v12
	v_exp_f32_e32 v32, v32
	v_exp_f32_e32 v13, v13
	v_cvt_pk_bf16_f32 v3, v3, v8
	v_exp_f32_e32 v8, v16
	v_add_co_u32_e32 v14, vcc, s49, v30
	v_cvt_pk_bf16_f32 v70, v6, v15
	s_nop 0
	v_addc_co_u32_e32 v15, vcc, 0, v31, vcc
	v_cvt_pk_bf16_f32 v2, v4, v2
	v_cvt_pk_bf16_f32 v4, v10, v9
	v_cvt_pk_bf16_f32 v68, v32, v12
	v_cvt_pk_bf16_f32 v69, v11, v7
	v_cvt_pk_bf16_f32 v71, v8, v13
	global_load_dwordx4 v[6:9], v[30:31], off offset:3072
	global_load_dwordx4 v[10:13], v[14:15], off
	s_waitcnt vmcnt(4)
	v_mfma_f32_32x32x16_bf16 v[50:65], v[26:29], v[2:5], 0
	global_load_dwordx4 v[72:75], v[14:15], off offset:3072
	v_add_f32_e32 v67, v66, v67
	v_cmp_gt_f32_e32 vcc, s69, v67
	s_cmp_eq_u64 vcc, exec
	s_cselect_b64 s[64:65], -1, 0
	s_cmpk_gt_i32 s42, 0xfe
	s_cselect_b64 s[72:73], -1, 0
	s_waitcnt vmcnt(3)
	v_mfma_f32_32x32x16_bf16 v[34:49], v[18:21], v[2:5], 0
	s_or_b64 s[64:65], s[72:73], s[64:65]
	s_and_b64 vcc, exec, s[64:65]
	v_mfma_f32_32x32x16_bf16 v[50:65], v[22:25], v[68:71], v[50:65]
	s_waitcnt vmcnt(2)
	v_mfma_f32_32x32x16_bf16 v[34:49], v[6:9], v[68:71], v[34:49]
	global_load_dwordx4 v[6:9], v[14:15], off offset:1024
	s_waitcnt vmcnt(2)
	v_mfma_f32_32x32x16_bf16 v[18:33], v[10:13], v[2:5], 0
	global_load_dwordx4 v[10:13], v[14:15], off offset:2048
	s_waitcnt vmcnt(1)
	v_mfma_f32_32x32x16_bf16 v[18:33], v[6:9], v[68:71], v[18:33]
	s_waitcnt vmcnt(0)
	v_mfma_f32_32x32x16_bf16 v[2:17], v[10:13], v[2:5], 0
	v_mfma_f32_32x32x16_bf16 v[2:17], v[72:75], v[68:71], v[2:17]
	s_cbranch_vccnz .LBB0_1655
	v_sub_u32_e64 v66, s43, 1 clamp
	s_sub_i32 s63, 0xfe, s42
	v_add_f32_e32 v147, 0, v67
	s_add_i32 s64, s42, 0xffffff02
	s_mov_b32 s92, s49
	s_mov_b32 s93, 0
	v_add_u32_e32 v252, s62, v66
	v_mov_b32_e32 v253, 0
	v_lshlrev_b64 v[252:253], 13, v[252:253]
	v_lshl_add_u64 v[252:253], v[140:141], 0, v[252:253]
	global_load_dwordx4 v[220:223], v[252:253], off
	global_load_dwordx4 v[224:227], v[252:253], off offset:1024
	global_load_dwordx4 v[228:231], v[252:253], off offset:2048
	global_load_dwordx4 v[232:235], v[252:253], off offset:3072
	v_lshl_add_u64 v[254:255], v[252:253], 0, s[92:93]
	global_load_dwordx4 v[236:239], v[254:255], off
	global_load_dwordx4 v[240:243], v[254:255], off offset:1024
	global_load_dwordx4 v[244:247], v[254:255], off offset:2048
	global_load_dwordx4 v[248:251], v[254:255], off offset:3072
.LBB0_1664:
	v_add_u32_e32 v138, s62, v66
	v_lshlrev_b64 v[66:67], 13, v[138:139]
	v_lshl_add_u64 v[132:133], v[140:141], 0, v[66:67]
	v_lshl_add_u64 v[130:131], v[142:143], 0, v[66:67]
	v_add_co_u32_e32 v180, vcc, s49, v130
	global_load_dwordx4 v[168:171], v[130:131], off
	global_load_dwordx4 v[118:121], v[130:131], off offset:1024
	global_load_dwordx4 v[134:137], v[130:131], off offset:2048
	s_mov_b64 s[42:43], vcc
	v_add_f32_e32 v149, 0, v147
	s_nop 0
	v_addc_co_u32_e64 v181, vcc, 0, v131, s[42:43]
	s_add_i32 s63, s63, -1
	s_waitcnt vmcnt(10)
	v_mfma_f32_32x32x16_bf16 v[66:81], v[220:223], v[82:85], 0
	s_waitcnt vmcnt(9)
	v_mfma_f32_32x32x16_bf16 v[66:81], v[224:227], v[86:89], v[66:81]
	s_waitcnt vmcnt(8)
	v_mfma_f32_32x32x16_bf16 v[66:81], v[228:231], v[90:93], v[66:81]
	s_waitcnt vmcnt(7)
	v_mfma_f32_32x32x16_bf16 v[66:81], v[232:235], v[94:97], v[66:81]
	s_waitcnt vmcnt(6)
	v_mfma_f32_32x32x16_bf16 v[66:81], v[236:239], v[98:101], v[66:81]
	s_waitcnt vmcnt(5)
	v_mfma_f32_32x32x16_bf16 v[66:81], v[240:243], v[102:105], v[66:81]
	global_load_dwordx4 v[122:125], v[130:131], off offset:3072
	s_waitcnt vmcnt(5)
	v_mfma_f32_32x32x16_bf16 v[66:81], v[244:247], v[106:109], v[66:81]
	global_load_dwordx4 v[176:179], v[180:181], off
	global_load_dwordx4 v[126:129], v[180:181], off offset:1024
	global_load_dwordx4 v[130:133], v[180:181], off offset:2048
	global_load_dwordx4 v[114:117], v[180:181], off offset:3072
	s_waitcnt vmcnt(8)
	v_mfma_f32_32x32x16_bf16 v[66:81], v[248:251], v[110:113], v[66:81]
	s_add_i32 s90, s62, s63
	s_max_i32 s90, s90, 0
	s_lshl_b32 s90, s90, 13
	s_mov_b32 s91, 0
	v_lshl_add_u64 v[252:253], v[140:141], 0, s[90:91]
	global_load_dwordx4 v[220:223], v[252:253], off
	global_load_dwordx4 v[224:227], v[252:253], off offset:1024
	global_load_dwordx4 v[228:231], v[252:253], off offset:2048
	global_load_dwordx4 v[232:235], v[252:253], off offset:3072
	v_lshl_add_u64 v[254:255], v[252:253], 0, s[92:93]
	global_load_dwordx4 v[236:239], v[254:255], off
	global_load_dwordx4 v[240:243], v[254:255], off offset:1024
	global_load_dwordx4 v[244:247], v[254:255], off offset:2048
	global_load_dwordx4 v[248:251], v[254:255], off offset:3072
	s_nop 11
	v_mul_f32_e32 v180, 0x3e0293ee, v75
	v_mul_f32_e32 v76, 0x3e0293ee, v76
	v_mul_f32_e32 v75, 0x3e0293ee, v77
	v_mul_f32_e32 v78, 0x3e0293ee, v78
	v_mul_f32_e32 v182, 0x3e0293ee, v79
	v_mul_f32_e32 v80, 0x3e0293ee, v80
	v_mul_f32_e32 v79, 0x3e0293ee, v81
	v_mul_f32_e32 v66, 0x3e0293ee, v66
	v_mul_f32_e32 v172, 0x3e0293ee, v67
	v_mul_f32_e32 v68, 0x3e0293ee, v68
	v_mul_f32_e32 v67, 0x3e0293ee, v69
	v_mul_f32_e32 v70, 0x3e0293ee, v70
	v_mul_f32_e32 v174, 0x3e0293ee, v71
	v_mul_f32_e32 v72, 0x3e0293ee, v72
	v_mul_f32_e32 v71, 0x3e0293ee, v73
	v_mul_f32_e32 v74, 0x3e0293ee, v74
	v_exp_f32_e64 v201, -|v180|
	v_exp_f32_e64 v202, -|v76|
	v_exp_f32_e64 v203, -|v75|
	v_max_f32_e32 v195, 0, v75
	v_exp_f32_e64 v75, -|v78|
	v_exp_f32_e64 v204, -|v182|
	v_exp_f32_e64 v205, -|v80|
	v_exp_f32_e64 v206, -|v79|
	v_exp_f32_e64 v138, -|v66|
	v_exp_f32_e64 v167, -|v172|
	v_exp_f32_e64 v173, -|v68|
	v_exp_f32_e64 v175, -|v67|
	v_max_f32_e32 v187, 0, v67
	v_exp_f32_e64 v67, -|v70|
	v_exp_f32_e64 v181, -|v174|
	v_exp_f32_e64 v183, -|v72|
	v_exp_f32_e64 v200, -|v71|
	v_max_f32_e32 v191, 0, v71
	v_exp_f32_e64 v71, -|v74|
	v_add_f32_e32 v209, 1.0, v201
	v_add_f32_e32 v211, 1.0, v202
	v_add_f32_e32 v212, 1.0, v203
	v_add_f32_e32 v75, 1.0, v75
	v_add_f32_e32 v213, 1.0, v204
	v_add_f32_e32 v215, 1.0, v205
	v_add_f32_e32 v216, 1.0, v206
	v_max_f32_e32 v199, 0, v79
	v_add_f32_e32 v79, 1.0, v138
	v_add_f32_e32 v138, 1.0, v167
	v_add_f32_e32 v167, 1.0, v173
	v_add_f32_e32 v173, 1.0, v175
	v_add_f32_e32 v67, 1.0, v67
	v_add_f32_e32 v175, 1.0, v181
	v_add_f32_e32 v181, 1.0, v183
	v_add_f32_e32 v183, 1.0, v200
	v_add_f32_e32 v71, 1.0, v71
	v_log_f32_e32 v210, v209
	v_log_f32_e32 v209, v211
	v_log_f32_e32 v211, v212
	v_log_f32_e32 v212, v75
	v_log_f32_e32 v214, v213
	v_log_f32_e32 v213, v215
	v_log_f32_e32 v215, v216
	v_log_f32_e32 v204, v67
	v_log_f32_e32 v206, v175
	v_log_f32_e32 v205, v181
	v_log_f32_e32 v207, v183
	v_log_f32_e32 v208, v71
	v_log_f32_e32 v202, v138
	v_log_f32_e32 v203, v173
	v_max_f32_e32 v196, 0, v78
	v_max_f32_e32 v198, 0, v182
	v_max_f32_e32 v197, 0, v80
	v_log_f32_e32 v200, v79
	v_log_f32_e32 v201, v167
	v_max_f32_e32 v188, 0, v70
	v_max_f32_e32 v190, 0, v174
	v_max_f32_e32 v189, 0, v72
	v_max_f32_e32 v192, 0, v74
	v_max_f32_e32 v194, 0, v180
	v_max_f32_e32 v193, 0, v76
	v_pk_add_f32 v[196:197], v[196:197], v[212:213]
	v_pk_add_f32 v[198:199], v[198:199], v[214:215]
	v_max_f32_e32 v186, 0, v172
	v_pk_add_f32 v[188:189], v[188:189], v[204:205]
	v_pk_add_f32 v[190:191], v[190:191], v[206:207]
	v_pk_add_f32 v[192:193], v[192:193], v[208:209]
	v_pk_add_f32 v[194:195], v[194:195], v[210:211]
	v_pk_add_f32 v[206:207], v[198:199], v[196:197] neg_lo:[1,1] neg_hi:[1,1]
	v_max_f32_e32 v184, 0, v66
	v_max_f32_e32 v185, 0, v68
	v_pk_add_f32 v[186:187], v[186:187], v[202:203]
	v_pk_add_f32 v[202:203], v[190:191], v[188:189] neg_lo:[1,1] neg_hi:[1,1]
	v_pk_add_f32 v[204:205], v[194:195], v[192:193] neg_lo:[1,1] neg_hi:[1,1]
	v_pk_add_f32 v[206:207], v[206:207], v[206:207] op_sel:[0,1] op_sel_hi:[1,0]
	v_pk_add_f32 v[184:185], v[184:185], v[200:201]
	v_pk_add_f32 v[202:203], v[202:203], v[202:203] op_sel:[0,1] op_sel_hi:[1,0]
	v_pk_add_f32 v[204:205], v[204:205], v[204:205] op_sel:[0,1] op_sel_hi:[1,0]
	v_mov_b32_e32 v219, v206
	v_pk_add_f32 v[200:201], v[186:187], v[184:185] neg_lo:[1,1] neg_hi:[1,1]
	v_mov_b32_e32 v75, v202
	v_mov_b32_e32 v218, v204
	v_permlane32_swap_b32_e32 v206, v219
	v_pk_add_f32 v[200:201], v[200:201], v[200:201] op_sel:[0,1] op_sel_hi:[1,0]
	v_permlane32_swap_b32_e32 v202, v75
	v_permlane32_swap_b32_e32 v204, v218
	v_mov_b32_e32 v205, v206
	v_add_f32_e32 v201, v202, v75
	v_pk_add_f32 v[202:203], v[204:205], v[218:219]
	v_fma_f32 v67, v69, s68, -v187
	v_fma_f32 v69, v73, s68, -v191
	v_fma_f32 v73, v81, s68, -v199
	v_mov_b32_e32 v216, v200
	v_cndmask_b32_e64 v81, 0, v219, s[6:7]
	v_pk_add_f32 v[204:205], v[202:203], v[202:203] op_sel:[0,1] op_sel_hi:[1,0]
	v_fma_f32 v71, v77, s68, -v195
	v_mov_b32_e32 v214, v197
	v_mov_b32_e32 v215, v199
	v_permlane32_swap_b32_e32 v200, v216
	v_cndmask_b32_e64 v77, 0, v218, s[6:7]
	v_add_f32_e32 v81, v149, v81
	v_add_f32_e32 v138, v147, v203
	v_mov_b32_e32 v217, v204
	v_cndmask_b32_e64 v75, 0, v75, s[6:7]
	v_pk_add_f32 v[202:203], v[80:81], v[214:215] neg_lo:[0,1] neg_hi:[0,1]
	v_add_f32_e32 v73, v73, v81
	v_add_f32_e32 v149, v147, v204
	v_add_f32_e32 v77, v77, v138
	v_pk_add_f32 v[80:81], v[200:201], v[216:217]
	v_mov_b32_e32 v210, v189
	v_mov_b32_e32 v211, v191
	v_mov_b32_e32 v212, v193
	v_mov_b32_e32 v213, v195
	v_cndmask_b32_e64 v79, 0, v216, s[6:7]
	v_exp_f32_e32 v138, v73
	v_add_f32_e32 v73, v75, v149
	v_add_f32_e32 v75, v71, v77
	v_add_f32_e32 v71, v147, v81
	v_mov_b32_e32 v208, v185
	v_mov_b32_e32 v209, v187
	v_pk_add_f32 v[200:201], v[76:77], v[212:213] neg_lo:[0,1] neg_hi:[0,1]
	v_pk_add_f32 v[76:77], v[72:73], v[210:211] neg_lo:[0,1] neg_hi:[0,1]
	v_add_f32_e32 v72, v69, v73
	v_add_f32_e32 v69, v79, v71
	v_mov_b32_e32 v191, v189
	v_mov_b32_e32 v175, v77
	v_add_f32_e32 v71, 0, v72
	v_add_f32_e32 v76, v76, v77
	v_pk_add_f32 v[72:73], v[68:69], v[208:209] neg_lo:[0,1] neg_hi:[0,1]
	v_mov_b32_e32 v187, v185
	v_add_f32_e32 v67, v67, v69
	v_pk_add_f32 v[68:69], v[174:175], v[190:191] neg_lo:[0,1] neg_hi:[0,1]
	v_add_f32_e32 v76, 0, v76
	v_mov_b32_e32 v173, v73
	v_exp_f32_e32 v77, v71
	v_add_f32_e32 v67, 0, v67
	v_add_f32_e32 v72, v72, v73
	v_mov_b32_e32 v71, v69
	v_exp_f32_e32 v73, v76
	v_add_f32_e32 v76, v68, v69
	v_pk_add_f32 v[68:69], v[172:173], v[186:187] neg_lo:[0,1] neg_hi:[0,1]
	v_mov_b32_e32 v185, v186
	v_exp_f32_e32 v79, v67
	v_mov_b32_e32 v67, v69
	v_mov_b32_e32 v189, v190
	v_pk_add_f32 v[66:67], v[66:67], v[184:185] neg_lo:[0,1] neg_hi:[0,1]
	v_pk_add_f32 v[70:71], v[70:71], v[188:189] neg_lo:[0,1] neg_hi:[0,1]
	v_add_f32_e32 v68, v68, v69
	v_add_f32_e32 v66, v66, v67
	v_add_f32_e32 v69, v70, v71
	v_add_f32_e32 v68, 0, v68
	v_add_f32_e32 v66, 0, v66
	v_add_f32_e32 v72, 0, v72
	v_add_f32_e32 v76, 0, v76
	v_add_f32_e32 v69, 0, v69
	v_exp_f32_e32 v70, v68
	v_exp_f32_e32 v66, v66
	v_exp_f32_e32 v72, v72
	v_exp_f32_e32 v76, v76
	v_exp_f32_e32 v68, v69
	v_mov_b32_e32 v199, v197
	v_mov_b32_e32 v183, v203
	v_mov_b32_e32 v195, v193
	v_cvt_pk_bf16_f32 v66, v66, v70
	v_pk_add_f32 v[70:71], v[182:183], v[198:199] neg_lo:[0,1] neg_hi:[0,1]
	v_mov_b32_e32 v181, v201
	v_mov_b32_e32 v197, v198
	v_cvt_pk_bf16_f32 v69, v73, v77
	v_cvt_pk_bf16_f32 v67, v72, v79
	v_cvt_pk_bf16_f32 v68, v68, v76
	v_add_f32_e32 v72, 0, v75
	v_add_f32_e32 v73, v200, v201
	v_mov_b32_e32 v79, v71
	v_add_f32_e32 v75, v70, v71
	v_pk_add_f32 v[70:71], v[180:181], v[194:195] neg_lo:[0,1] neg_hi:[0,1]
	v_mov_b32_e32 v193, v194
	s_waitcnt vmcnt(13)
	v_mfma_f32_32x32x16_bf16 v[34:49], v[134:137], v[66:69], v[34:49]
	v_exp_f32_e32 v77, v72
	v_add_f32_e32 v134, 0, v73
	v_pk_add_f32 v[72:73], v[78:79], v[196:197] neg_lo:[0,1] neg_hi:[0,1]
	v_exp_f32_e32 v78, v75
	v_mov_b32_e32 v75, v71
	v_add_f32_e32 v70, v70, v71
	v_add_f32_e32 v71, v72, v73
	v_mfma_f32_32x32x16_bf16 v[50:65], v[168:171], v[66:69], v[50:65]
	v_add_f32_e64 v72, v74, -v192
	v_add_f32_e64 v73, v75, -v193
	v_add_f32_e32 v167, v202, v203
	v_add_f32_e32 v70, 0, v70
	v_exp_f32_e32 v76, v167
	v_exp_f32_e32 v79, v134
	v_exp_f32_e32 v74, v71
	v_exp_f32_e32 v75, v70
	s_waitcnt vmcnt(11)
	v_mfma_f32_32x32x16_bf16 v[18:33], v[176:179], v[66:69], v[18:33]
	v_cvt_pk_bf16_f32 v71, v76, v138
	v_cvt_pk_bf16_f32 v70, v74, v78
	s_waitcnt vmcnt(9)
	v_mfma_f32_32x32x16_bf16 v[2:17], v[130:133], v[66:69], v[2:17]
	v_add_f32_e32 v66, v72, v73
	v_add_f32_e32 v66, 0, v66
	v_exp_f32_e32 v66, v66
	v_cvt_pk_bf16_f32 v69, v79, v77
	v_add_f32_e32 v67, v80, v81
	v_add_f32_e32 v147, v147, v67
	v_cvt_pk_bf16_f32 v68, v66, v75
	v_cmp_gt_f32_e32 vcc, s69, v147
	s_cmp_lg_u64 vcc, exec
	v_mfma_f32_32x32x16_bf16 v[50:65], v[118:121], v[68:71], v[50:65]
	s_cselect_b64 s[42:43], -1, 0
	s_cmp_lg_u32 s64, 0
	s_cselect_b64 s[72:73], -1, 0
	s_and_b64 s[42:43], s[72:73], s[42:43]
	v_mov_b32_e32 v66, s63
	s_add_i32 s64, s64, 1
	s_and_b64 vcc, exec, s[42:43]
	v_mfma_f32_32x32x16_bf16 v[34:49], v[122:125], v[68:71], v[34:49]
	v_mfma_f32_32x32x16_bf16 v[18:33], v[126:129], v[68:71], v[18:33]
	s_waitcnt vmcnt(8)
	v_mfma_f32_32x32x16_bf16 v[2:17], v[114:117], v[68:71], v[2:17]
	s_cbranch_vccnz .LBB0_1664
	s_branch .LBB0_1655
